# early-3-tiles prologue + ring loop + one static s_setprio 1 for waves 4-7 during the streaming loop
# speedup vs baseline: 1.0280x; 1.0280x over previous
.LBB1_8:
	s_or_b64 exec, exec, s[2:3]
	s_nop 4
	v_lshlrev_b32_e32 v156, 11, v197
	v_lshl_or_b32 v156, v184, 2, v156
	s_waitcnt lgkmcnt(0)
	s_barrier
	ds_read_b128 v[10:13], v156 offset:16640
	ds_read_b128 v[6:9], v156 offset:17664
	v_and_b32_e32 v2, 8, v0
	v_cmp_eq_u32_e64 s[4:5], 0, v2
	v_and_b32_e32 v2, 4, v0
	s_load_dwordx2 s[18:19], s[0:1], 0x70
	v_cmp_eq_u32_e64 s[2:3], 0, v2
	v_and_b32_e32 v2, 3, v0
	s_movk_i32 s0, 0x320
	v_cmp_eq_u32_e32 vcc, 0, v2
	v_mad_i64_i32 v[2:3], s[0:1], v104, s0, 0
	v_or_b32_e32 v2, v2, v108
	v_bfe_u32 v109, v0, 2, 1
	v_lshl_add_u64 v[2:3], s[16:17], 0, v[2:3]
	v_lshl_add_u64 v[118:119], v[2:3], 0, 64
	v_lshl_add_u64 v[118:119], v[118:119], 0, 32
	v_mul_u32_u24_e32 v2, 0x320, v109
	s_movk_i32 s0, 0x640
	v_mad_u32_u24 v2, v197, s0, v2
	v_and_b32_e32 v199, 31, v0
	v_or_b32_e32 v2, v2, v108
	v_lshlrev_b32_e32 v186, 4, v199
	v_mov_b32_e32 v187, 0
	v_add_u32_e32 v114, 0x8200, v2
	v_lshl_add_u64 v[2:3], v[78:79], 0, v[186:187]
	v_lshl_add_u64 v[2:3], v[102:103], 0, v[2:3]
	s_mov_b64 s[0:1], 0x3000
	v_add_u32_e32 v201, 0xe500, v105
	v_lshl_add_u64 v[116:117], v[2:3], 0, s[0:1]
	v_mov_b32_e32 v104, 0xff800000
	v_mov_b32_e32 v113, 0xd01502f9
	s_mov_b64 s[16:17], 0x1000
	v_mov_b32_e32 v96, 0
	v_mov_b32_e32 v97, 0
	v_mov_b32_e32 v98, 0
	v_mov_b32_e32 v99, 0
	v_mov_b32_e32 v100, 0
	v_mov_b32_e32 v101, 0
	v_mov_b32_e32 v102, 0
	v_mov_b32_e32 v103, 0
	v_mov_b32_e32 v105, 0
	s_mov_b32 s30, 0
	global_load_dword v205, v[118:119], off nt
	global_load_dwordx4 v[138:141], v[116:117], off nt
	global_load_dwordx4 v[146:149], v[116:117], off offset:512 nt
	global_load_dwordx4 v[152:155], v[116:117], off offset:1024 nt
	global_load_dwordx4 v[156:159], v[116:117], off offset:1536 nt
	global_load_dwordx4 v[160:163], v[116:117], off offset:2048 nt
	global_load_dwordx4 v[164:167], v[116:117], off offset:2560 nt
	global_load_dwordx4 v[168:171], v[116:117], off offset:3072 nt
	global_load_dwordx4 v[172:175], v[116:117], off offset:3584 nt
	v_lshl_add_u64 v[116:117], v[116:117], 0, s[16:17]
	v_lshl_add_u64 v[118:119], v[118:119], 0, 32
	v_readfirstlane_b32 s32, v197
	s_nop 3
	s_cmp_lt_u32 s32, 4
	s_cbranch_scc1 .Lring_prio_done
	s_setprio 1
.Lring_prio_done:
	s_waitcnt lgkmcnt(0)

.Lring_done:
	s_setprio 0
	v_mov_b32_e32 v240, v96
	v_mov_b32_e32 v241, v97
	v_mov_b32_e32 v242, v98
	v_mov_b32_e32 v243, v99
	v_mov_b32_e32 v244, v100
	v_mov_b32_e32 v245, v101
	v_mov_b32_e32 v246, v102
	v_mov_b32_e32 v247, v103
	v_mov_b32_e32 v248, v104
	v_mov_b32_e32 v249, v105
	s_movk_i32 s0, 0x640
	v_mov_b32_e32 v14, 0x8200
	v_mad_u32_u24 v205, v197, s0, v14
	v_lshlrev_b32_e32 v10, 4, v106
	v_or_b32_e32 v6, 0x2000, v196
	v_add_lshl_u32 v7, v122, v6, 4
	global_load_dwordx4 v[158:161], v10, s[8:9]
	global_load_dwordx4 v[154:157], v10, s[8:9] offset:1024
	global_load_dwordx4 v[146:149], v10, s[8:9] offset:2048
	global_load_dwordx4 v[138:141], v10, s[8:9] offset:3072
	global_load_dwordx4 v[118:121], v131, s[8:9]
	global_load_dwordx4 v[106:109], v132, s[8:9]
	global_load_dwordx4 v[98:101], v133, s[8:9]
	global_load_dwordx4 v[102:105], v134, s[8:9]
	global_load_dwordx4 v[170:173], v135, s[8:9]
	global_load_dwordx4 v[166:169], v137, s[8:9]
	global_load_dwordx4 v[178:181], v136, s[8:9]
	global_load_dwordx4 v[174:177], v142, s[8:9]
	global_load_dwordx4 v[162:165], v143, s[8:9]
	s_nop 0
	global_load_dwordx4 v[134:137], v144, s[8:9]
	global_load_dwordx4 v[114:117], v145, s[8:9]
	global_load_dwordx4 v[110:113], v150, s[8:9]
	global_load_dwordx4 v[94:97], v7, s[8:9]
	global_load_dwordx4 v[90:93], v7, s[8:9] offset:1024
	global_load_dwordx4 v[78:81], v7, s[8:9] offset:2048
	global_load_dwordx4 v[74:77], v7, s[8:9] offset:3072
	v_add_lshl_u32 v7, v123, v6, 4
	v_add_lshl_u32 v8, v124, v6, 4
	global_load_dwordx4 v[66:69], v7, s[8:9]
	global_load_dwordx4 v[58:61], v8, s[8:9]
	v_add_lshl_u32 v7, v125, v6, 4
	v_add_lshl_u32 v8, v126, v6, 4
	global_load_dwordx4 v[62:65], v7, s[8:9]
	global_load_dwordx4 v[54:57], v8, s[8:9]
	v_add_lshl_u32 v7, v127, v6, 4
	v_add_lshl_u32 v8, v128, v6, 4
	global_load_dwordx4 v[150:153], v7, s[8:9]
	global_load_dwordx4 v[142:145], v8, s[8:9]
	v_add_lshl_u32 v7, v129, v6, 4
	v_add_lshl_u32 v8, v130, v6, 4
	global_load_dwordx4 v[130:133], v7, s[8:9]
	global_load_dwordx4 v[126:129], v8, s[8:9]
	v_add_lshl_u32 v7, v192, v6, 4
	v_add_lshl_u32 v8, v202, v6, 4
	global_load_dwordx4 v[122:125], v7, s[8:9]
	global_load_dwordx4 v[82:85], v8, s[8:9]
	v_add_lshl_u32 v7, v203, v6, 4
	v_add_lshl_u32 v6, v204, v6, 4
	global_load_dwordx4 v[86:89], v7, s[8:9]
	global_load_dwordx4 v[70:73], v6, s[8:9]
	v_lshlrev_b32_e32 v187, 2, v195
	v_and_or_b32 v190, v187, 4, s31
	v_or_b32_e32 v208, 1, v190
	v_mul_u32_u24_e32 v6, 0x300, v197
	v_ashrrev_i32_e32 v191, 31, v190
	v_ashrrev_i32_e32 v209, 31, v208
	v_or_b32_e32 v6, v196, v6
	v_lshlrev_b64 v[210:211], 9, v[190:191]
	v_lshlrev_b32_e32 v191, 2, v1
	v_lshlrev_b64 v[222:223], 9, v[208:209]
	v_or_b32_e32 v208, 2, v190
	v_mov_b32_e32 v193, 0
	v_lshlrev_b32_e32 v14, 4, v6
	v_lshl_or_b32 v192, v197, 7, v191
	s_movk_i32 s2, 0xfe00
	v_ashrrev_i32_e32 v209, 31, v208
	v_or_b32_e32 v6, 0x40000, v14
	s_movk_i32 s1, 0x100
	v_lshl_add_u64 v[220:221], s[22:23], 0, v[192:193]
	s_mov_b32 s3, -1
	v_lshlrev_b64 v[226:227], 9, v[208:209]
	v_or_b32_e32 v208, 3, v190
	global_load_dwordx4 v[50:53], v6, s[8:9]
	global_load_dwordx4 v[46:49], v6, s[8:9] offset:1024
	global_load_dwordx4 v[42:45], v6, s[8:9] offset:2048
	global_load_dwordx4 v[30:33], v6, s[8:9] offset:3072
	v_add_u32_e32 v6, 0x41000, v14
	v_add_u32_e32 v7, 0x41400, v14
	v_lshl_add_u64 v[212:213], s[20:21], 0, v[192:193]
	v_lshl_add_u64 v[202:203], v[220:221], 0, s[2:3]
	v_cmp_gt_u32_e32 vcc, s1, v0
	v_ashrrev_i32_e32 v209, 31, v208
	s_movk_i32 s2, 0xfe40
	global_load_dwordx4 v[38:41], v6, s[8:9]
	global_load_dwordx4 v[22:25], v7, s[8:9]
	v_add_u32_e32 v6, 0x41800, v14
	v_add_u32_e32 v7, 0x41c00, v14
	v_cndmask_b32_e32 v203, v203, v213, vcc
	v_cndmask_b32_e32 v202, v202, v212, vcc
	v_lshlrev_b64 v[230:231], 9, v[208:209]
	s_mov_b32 s3, -1
	global_load_dwordx4 v[34:37], v6, s[8:9]
	global_load_dwordx4 v[10:13], v7, s[8:9]
	v_add_u32_e32 v6, 0x42000, v14
	v_add_u32_e32 v7, 0x42400, v14
	v_add_u32_e32 v15, 0x42800, v14
	v_add_u32_e32 v18, 0x42c00, v14
	v_lshl_add_u64 v[206:207], v[202:203], 0, v[210:211]
	v_lshl_add_u64 v[224:225], v[202:203], 0, v[222:223]
	v_lshl_add_u64 v[228:229], v[202:203], 0, v[226:227]
	v_lshl_add_u64 v[202:203], v[202:203], 0, v[230:231]
	v_lshl_add_u64 v[212:213], v[212:213], 0, 64
	v_lshl_add_u64 v[220:221], v[220:221], 0, s[2:3]
	global_load_dwordx4 v[26:29], v6, s[8:9]
	s_nop 0
	global_load_dwordx4 v[6:9], v7, s[8:9]
	s_nop 0
	global_load_dwordx4 v[14:17], v15, s[8:9]
	s_nop 0
	global_load_dwordx4 v[18:21], v18, s[8:9]
	s_nop 0
	global_load_dword v208, v[206:207], off
	s_nop 0
	global_load_dword v207, v[224:225], off
	global_load_dword v204, v[228:229], off
	s_nop 0
	global_load_dword v203, v[202:203], off
	s_nop 0
	global_load_dword v206, v192, s[10:11]
	global_load_dword v202, v192, s[10:11] offset:64
	v_cndmask_b32_e32 v213, v221, v213, vcc
	v_cndmask_b32_e32 v212, v220, v212, vcc
	v_lshl_add_u64 v[210:211], v[212:213], 0, v[210:211]
	v_lshl_add_u64 v[220:221], v[212:213], 0, v[222:223]
	v_lshl_add_u64 v[222:223], v[212:213], 0, v[226:227]
	v_lshl_add_u64 v[224:225], v[212:213], 0, v[230:231]
	global_load_dword v212, v[210:211], off
	s_nop 0
	global_load_dword v211, v[220:221], off
	global_load_dword v210, v[222:223], off
	global_load_dword v209, v[224:225], off
	v_lshl_or_b32 v190, v197, 4, v1
	v_lshlrev_b32_e32 v186, 2, v190
	global_load_dword v189, v186, s[24:25]
	global_load_dword v188, v186, s[26:27]
	v_mov_b32_e32 v233, v249
	v_mov_b32_e32 v232, v248
	v_mov_b32_e32 v214, v240
	v_mov_b32_e32 v215, v241
	v_mov_b32_e32 v216, v242
	v_mov_b32_e32 v217, v243
	v_mov_b32_e32 v218, v244
	v_mov_b32_e32 v219, v245
	v_mov_b32_e32 v220, v246
	v_mov_b32_e32 v221, v247
	s_nop 1
	v_add_f32_dpp v2, v233, v233 row_ror:8 row_mask:0xf bank_mask:0xf bound_ctrl:1
	v_mov_b32_e32 v3, v2
	s_nop 1
	v_permlane16_swap_b32_e32 v2, v3
	v_add_f32_e32 v2, v2, v3
	v_mov_b32_e32 v3, v2
	s_nop 1
	v_permlane32_swap_b32_e32 v2, v3
	v_add_f32_e32 v2, v2, v3
	v_readlane_b32 s2, v232, 4
	v_readlane_b32 s4, v2, 4
	v_readlane_b32 s5, v2, 0
	v_readlane_b32 s3, v232, 0
	v_div_scale_f32 v3, s[0:1], s4, s4, 1.0
	v_rcp_f32_e32 v4, v3
	v_lshl_add_u64 v[182:183], v[182:183], 2, s[28:29]
	v_fma_f32 v2, -v3, v4, 1.0
	v_fmac_f32_e32 v4, v2, v4
	v_div_scale_f32 v2, vcc, 1.0, s4, 1.0
	v_mul_f32_e32 v5, v2, v4
	v_fma_f32 v192, -v3, v5, v2
	v_fmac_f32_e32 v5, v192, v4
	v_fma_f32 v2, -v3, v5, v2
	v_div_scale_f32 v3, s[0:1], s5, s5, 1.0
	v_rcp_f32_e32 v192, v3
	v_div_fmas_f32 v2, v2, v4, v5
	v_div_fixup_f32 v2, v2, s4, 1.0
	s_movk_i32 s0, 0xc8
	v_fma_f32 v4, -v3, v192, 1.0
	v_fmac_f32_e32 v192, v4, v192
	v_div_scale_f32 v4, vcc, 1.0, s5, 1.0
	v_mul_f32_e32 v5, v4, v192
	v_fma_f32 v213, -v3, v5, v4
	v_fmac_f32_e32 v5, v213, v192
	v_fma_f32 v3, -v3, v5, v4
	v_div_fmas_f32 v3, v3, v192, v5
	v_div_fixup_f32 v4, v3, s5, 1.0
	v_pk_mul_f32 v[216:217], v[216:217], v[4:5] op_sel_hi:[1,0]
	v_pk_mul_f32 v[214:215], v[214:215], v[4:5] op_sel_hi:[1,0]
	v_cvt_pk_f16_f32 v217, v216, v217
	v_cvt_pk_f16_f32 v216, v214, v215
	v_pk_mul_f32 v[214:215], v[220:221], v[2:3] op_sel_hi:[1,0]
	v_pk_mul_f32 v[218:219], v[218:219], v[2:3] op_sel_hi:[1,0]
	v_add_u32_e32 v3, v205, v184
	ds_read2_b32 v[220:221], v3 offset0:128 offset1:200
	v_cvt_pk_f16_f32 v215, v214, v215
	v_cvt_pk_f16_f32 v214, v218, v219
	ds_read2st64_b32 v[218:219], v3 offset1:1
	v_add_u32_e32 v192, 32, v3
	ds_write2st64_b64 v185, v[216:217], v[214:215] offset1:1
	ds_read2st64_b32 v[214:215], v192 offset0:4 offset1:5
	s_waitcnt lgkmcnt(3)
	v_subrev_f32_e32 v5, s2, v221
	v_exp_f32_e32 v5, v5
	s_waitcnt lgkmcnt(2)
	v_subrev_f32_e32 v185, s3, v218
	v_exp_f32_e32 v185, v185
	s_waitcnt lgkmcnt(0)
	v_subrev_f32_e32 v205, s2, v214
	v_mul_f32_e32 v5, v2, v5
	v_subrev_f32_e32 v192, s3, v219
	v_exp_f32_e32 v205, v205
	v_fmac_f32_e32 v5, v4, v185
	v_mov_b32_e32 v185, v193
	v_exp_f32_e32 v192, v192
	v_lshl_add_u64 v[182:183], v[182:183], 0, v[184:185]
	v_subrev_f32_e32 v185, s2, v215
	v_mul_f32_e32 v5, 0.5, v5
	v_subrev_f32_e32 v184, s3, v220
	v_exp_f32_e32 v185, v185
	global_store_dword v[182:183], v5, off
	v_mul_f32_e32 v5, v2, v205
	v_exp_f32_e32 v184, v184
	v_fmac_f32_e32 v5, v4, v192
	v_mul_f32_e32 v5, 0.5, v5
	global_store_dword v[182:183], v5, off offset:256
	v_mul_f32_e32 v5, v2, v185
	v_fmac_f32_e32 v5, v4, v184
	v_mul_f32_e32 v5, 0.5, v5
	global_store_dword v[182:183], v5, off offset:512
	v_or_b32_e32 v5, 0xc0, v196
	v_cmp_gt_u32_e32 vcc, s0, v5
	s_and_saveexec_b64 s[0:1], vcc
	s_cbranch_execz .LBB1_19
	v_add_u32_e32 v3, 0x300, v3
	ds_read2_b32 v[184:185], v3 offset1:200
	s_waitcnt lgkmcnt(0)
	v_subrev_f32_e32 v3, s3, v184
	v_subrev_f32_e32 v5, s2, v185
	v_exp_f32_e32 v184, v3
	v_exp_f32_e32 v185, v5
	v_mov_b32_e32 v5, v2
	v_pk_mul_f32 v[2:3], v[4:5], v[184:185]
	s_nop 0
	v_add_f32_e32 v2, v2, v3
	v_mul_f32_e32 v2, 0.5, v2
	global_store_dword v[182:183], v2, off offset:768
